# speedup vs baseline: 1.0317x; 1.0041x over previous
.LBB4_6:
	s_or_b64 exec, exec, s[0:1]
	v_add_u32_e32 v0, 0x20000, v215
	ds_read_b64 v[16:17], v0
	s_waitcnt lgkmcnt(0)
	v_cvt_f32_f16_e32 v9, v16
	v_cvt_f32_f16_sdwa v10, v16 dst_sel:DWORD dst_unused:UNUSED_PAD src0_sel:WORD_1
	v_cvt_f32_f16_e32 v11, v17
	v_cvt_f32_f16_sdwa v12, v17 dst_sel:DWORD dst_unused:UNUSED_PAD src0_sel:WORD_1
	global_store_dwordx2 v[2:3], v[16:17], off offset:1056
	v_max_f32_dpp v9, v9, v9 quad_perm:[1,0,3,2] row_mask:0xf bank_mask:0xf
	v_max_f32_dpp v10, v10, v10 quad_perm:[1,0,3,2] row_mask:0xf bank_mask:0xf
	v_max_f32_dpp v11, v11, v11 quad_perm:[1,0,3,2] row_mask:0xf bank_mask:0xf
	v_max_f32_dpp v12, v12, v12 quad_perm:[1,0,3,2] row_mask:0xf bank_mask:0xf
	v_max_f32_dpp v9, v9, v9 quad_perm:[2,3,0,1] row_mask:0xf bank_mask:0xf
	v_max_f32_dpp v10, v10, v10 quad_perm:[2,3,0,1] row_mask:0xf bank_mask:0xf
	v_max_f32_dpp v11, v11, v11 quad_perm:[2,3,0,1] row_mask:0xf bank_mask:0xf
	v_max_f32_dpp v12, v12, v12 quad_perm:[2,3,0,1] row_mask:0xf bank_mask:0xf
	v_max_f32_dpp v9, v9, v9 row_half_mirror row_mask:0xf bank_mask:0xf
	v_max_f32_dpp v10, v10, v10 row_half_mirror row_mask:0xf bank_mask:0xf
	v_max_f32_dpp v11, v11, v11 row_half_mirror row_mask:0xf bank_mask:0xf
	v_max_f32_dpp v12, v12, v12 row_half_mirror row_mask:0xf bank_mask:0xf
	s_and_saveexec_b64 s[0:1], vcc
	s_cbranch_execz .LBB4_8
	v_cvt_pk_f16_f32 v10, v9, v10
	v_cvt_pk_f16_f32 v11, v11, v12
	global_store_dwordx2 v[4:5], v[10:11], off offset:1056
.LBB4_8:
	s_or_b64 exec, exec, s[0:1]
	v_add_u32_e32 v0, 0x20000, v211
	ds_read_b64 v[16:17], v0
	s_waitcnt lgkmcnt(0)
	v_cvt_f32_f16_e32 v9, v16
	v_cvt_f32_f16_sdwa v10, v16 dst_sel:DWORD dst_unused:UNUSED_PAD src0_sel:WORD_1
	v_cvt_f32_f16_e32 v11, v17
	v_cvt_f32_f16_sdwa v12, v17 dst_sel:DWORD dst_unused:UNUSED_PAD src0_sel:WORD_1
	global_store_dwordx2 v[2:3], v[16:17], off offset:1088
	v_max_f32_dpp v9, v9, v9 quad_perm:[1,0,3,2] row_mask:0xf bank_mask:0xf
	v_max_f32_dpp v10, v10, v10 quad_perm:[1,0,3,2] row_mask:0xf bank_mask:0xf
	v_max_f32_dpp v11, v11, v11 quad_perm:[1,0,3,2] row_mask:0xf bank_mask:0xf
	v_max_f32_dpp v12, v12, v12 quad_perm:[1,0,3,2] row_mask:0xf bank_mask:0xf
	v_max_f32_dpp v9, v9, v9 quad_perm:[2,3,0,1] row_mask:0xf bank_mask:0xf
	v_max_f32_dpp v10, v10, v10 quad_perm:[2,3,0,1] row_mask:0xf bank_mask:0xf
	v_max_f32_dpp v11, v11, v11 quad_perm:[2,3,0,1] row_mask:0xf bank_mask:0xf
	v_max_f32_dpp v12, v12, v12 quad_perm:[2,3,0,1] row_mask:0xf bank_mask:0xf
	v_max_f32_dpp v9, v9, v9 row_half_mirror row_mask:0xf bank_mask:0xf
	v_max_f32_dpp v10, v10, v10 row_half_mirror row_mask:0xf bank_mask:0xf
	v_max_f32_dpp v11, v11, v11 row_half_mirror row_mask:0xf bank_mask:0xf
	v_max_f32_dpp v12, v12, v12 row_half_mirror row_mask:0xf bank_mask:0xf
	s_and_saveexec_b64 s[0:1], vcc
	s_cbranch_execz .LBB4_10
	v_cvt_pk_f16_f32 v10, v9, v10
	v_cvt_pk_f16_f32 v11, v11, v12
	global_store_dwordx2 v[4:5], v[10:11], off offset:1088
.LBB4_10:
	s_or_b64 exec, exec, s[0:1]
	v_add_u32_e32 v0, 0x20000, v212
	ds_read_b64 v[16:17], v0
	s_waitcnt lgkmcnt(0)
	v_cvt_f32_f16_e32 v9, v16
	v_cvt_f32_f16_sdwa v10, v16 dst_sel:DWORD dst_unused:UNUSED_PAD src0_sel:WORD_1
	v_cvt_f32_f16_e32 v11, v17
	v_cvt_f32_f16_sdwa v12, v17 dst_sel:DWORD dst_unused:UNUSED_PAD src0_sel:WORD_1
	global_store_dwordx2 v[2:3], v[16:17], off offset:1120
	v_max_f32_dpp v9, v9, v9 quad_perm:[1,0,3,2] row_mask:0xf bank_mask:0xf
	v_max_f32_dpp v10, v10, v10 quad_perm:[1,0,3,2] row_mask:0xf bank_mask:0xf
	v_max_f32_dpp v11, v11, v11 quad_perm:[1,0,3,2] row_mask:0xf bank_mask:0xf
	v_max_f32_dpp v12, v12, v12 quad_perm:[1,0,3,2] row_mask:0xf bank_mask:0xf
	v_max_f32_dpp v9, v9, v9 quad_perm:[2,3,0,1] row_mask:0xf bank_mask:0xf
	v_max_f32_dpp v10, v10, v10 quad_perm:[2,3,0,1] row_mask:0xf bank_mask:0xf
	v_max_f32_dpp v11, v11, v11 quad_perm:[2,3,0,1] row_mask:0xf bank_mask:0xf
	v_max_f32_dpp v12, v12, v12 quad_perm:[2,3,0,1] row_mask:0xf bank_mask:0xf
	v_max_f32_dpp v9, v9, v9 row_half_mirror row_mask:0xf bank_mask:0xf
	v_max_f32_dpp v10, v10, v10 row_half_mirror row_mask:0xf bank_mask:0xf
	v_max_f32_dpp v11, v11, v11 row_half_mirror row_mask:0xf bank_mask:0xf
	v_max_f32_dpp v12, v12, v12 row_half_mirror row_mask:0xf bank_mask:0xf
	s_and_saveexec_b64 s[0:1], vcc
	s_cbranch_execz .LBB4_12
	v_cvt_pk_f16_f32 v10, v9, v10
	v_cvt_pk_f16_f32 v11, v11, v12
	global_store_dwordx2 v[4:5], v[10:11], off offset:1120
.LBB4_12:
	s_or_b64 exec, exec, s[0:1]
	v_add_u32_e32 v0, 0x20000, v210
	ds_read_b64 v[16:17], v0
	s_waitcnt lgkmcnt(0)
	v_cvt_f32_f16_e32 v9, v16
	v_cvt_f32_f16_sdwa v10, v16 dst_sel:DWORD dst_unused:UNUSED_PAD src0_sel:WORD_1
	v_cvt_f32_f16_e32 v11, v17
	v_cvt_f32_f16_sdwa v12, v17 dst_sel:DWORD dst_unused:UNUSED_PAD src0_sel:WORD_1
	global_store_dwordx2 v[2:3], v[16:17], off offset:1152
	v_max_f32_dpp v9, v9, v9 quad_perm:[1,0,3,2] row_mask:0xf bank_mask:0xf
	v_max_f32_dpp v10, v10, v10 quad_perm:[1,0,3,2] row_mask:0xf bank_mask:0xf
	v_max_f32_dpp v11, v11, v11 quad_perm:[1,0,3,2] row_mask:0xf bank_mask:0xf
	v_max_f32_dpp v12, v12, v12 quad_perm:[1,0,3,2] row_mask:0xf bank_mask:0xf
	v_max_f32_dpp v9, v9, v9 quad_perm:[2,3,0,1] row_mask:0xf bank_mask:0xf
	v_max_f32_dpp v10, v10, v10 quad_perm:[2,3,0,1] row_mask:0xf bank_mask:0xf
	v_max_f32_dpp v11, v11, v11 quad_perm:[2,3,0,1] row_mask:0xf bank_mask:0xf
	v_max_f32_dpp v12, v12, v12 quad_perm:[2,3,0,1] row_mask:0xf bank_mask:0xf
	v_max_f32_dpp v9, v9, v9 row_half_mirror row_mask:0xf bank_mask:0xf
	v_max_f32_dpp v10, v10, v10 row_half_mirror row_mask:0xf bank_mask:0xf
	v_max_f32_dpp v11, v11, v11 row_half_mirror row_mask:0xf bank_mask:0xf
	v_max_f32_dpp v12, v12, v12 row_half_mirror row_mask:0xf bank_mask:0xf
	s_and_saveexec_b64 s[0:1], vcc
	s_cbranch_execz .LBB4_14
	v_cvt_pk_f16_f32 v10, v9, v10
	v_cvt_pk_f16_f32 v11, v11, v12
	global_store_dwordx2 v[4:5], v[10:11], off offset:1152
.LBB4_14:
	s_or_b64 exec, exec, s[0:1]
	v_add_u32_e32 v0, 0x20000, v1
	ds_read_b64 v[16:17], v0
	s_waitcnt lgkmcnt(0)
	v_cvt_f32_f16_e32 v9, v16
	v_cvt_f32_f16_sdwa v10, v16 dst_sel:DWORD dst_unused:UNUSED_PAD src0_sel:WORD_1
	v_cvt_f32_f16_e32 v11, v17
	v_cvt_f32_f16_sdwa v12, v17 dst_sel:DWORD dst_unused:UNUSED_PAD src0_sel:WORD_1
	global_store_dwordx2 v[2:3], v[16:17], off offset:1184
	v_max_f32_dpp v9, v9, v9 quad_perm:[1,0,3,2] row_mask:0xf bank_mask:0xf
	v_max_f32_dpp v10, v10, v10 quad_perm:[1,0,3,2] row_mask:0xf bank_mask:0xf
	v_max_f32_dpp v11, v11, v11 quad_perm:[1,0,3,2] row_mask:0xf bank_mask:0xf
	v_max_f32_dpp v12, v12, v12 quad_perm:[1,0,3,2] row_mask:0xf bank_mask:0xf
	v_max_f32_dpp v9, v9, v9 quad_perm:[2,3,0,1] row_mask:0xf bank_mask:0xf
	v_max_f32_dpp v10, v10, v10 quad_perm:[2,3,0,1] row_mask:0xf bank_mask:0xf
	v_max_f32_dpp v11, v11, v11 quad_perm:[2,3,0,1] row_mask:0xf bank_mask:0xf
	v_max_f32_dpp v12, v12, v12 quad_perm:[2,3,0,1] row_mask:0xf bank_mask:0xf
	v_max_f32_dpp v9, v9, v9 row_half_mirror row_mask:0xf bank_mask:0xf
	v_max_f32_dpp v10, v10, v10 row_half_mirror row_mask:0xf bank_mask:0xf
	v_max_f32_dpp v11, v11, v11 row_half_mirror row_mask:0xf bank_mask:0xf
	v_max_f32_dpp v12, v12, v12 row_half_mirror row_mask:0xf bank_mask:0xf
	s_and_saveexec_b64 s[0:1], vcc
	s_cbranch_execz .LBB4_16
	v_cvt_pk_f16_f32 v10, v9, v10
	v_cvt_pk_f16_f32 v11, v11, v12
	global_store_dwordx2 v[4:5], v[10:11], off offset:1184
.LBB4_16:
	s_or_b64 exec, exec, s[0:1]
	v_add_u32_e32 v0, 0x20000, v216
	ds_read_b64 v[16:17], v0
	s_waitcnt lgkmcnt(0)
	v_cvt_f32_f16_e32 v9, v16
	v_cvt_f32_f16_sdwa v10, v16 dst_sel:DWORD dst_unused:UNUSED_PAD src0_sel:WORD_1
	v_cvt_f32_f16_e32 v11, v17
	v_cvt_f32_f16_sdwa v12, v17 dst_sel:DWORD dst_unused:UNUSED_PAD src0_sel:WORD_1
	global_store_dwordx2 v[2:3], v[16:17], off offset:1216
	v_max_f32_dpp v9, v9, v9 quad_perm:[1,0,3,2] row_mask:0xf bank_mask:0xf
	v_max_f32_dpp v10, v10, v10 quad_perm:[1,0,3,2] row_mask:0xf bank_mask:0xf
	v_max_f32_dpp v11, v11, v11 quad_perm:[1,0,3,2] row_mask:0xf bank_mask:0xf
	v_max_f32_dpp v12, v12, v12 quad_perm:[1,0,3,2] row_mask:0xf bank_mask:0xf
	v_max_f32_dpp v9, v9, v9 quad_perm:[2,3,0,1] row_mask:0xf bank_mask:0xf
	v_max_f32_dpp v10, v10, v10 quad_perm:[2,3,0,1] row_mask:0xf bank_mask:0xf
	v_max_f32_dpp v11, v11, v11 quad_perm:[2,3,0,1] row_mask:0xf bank_mask:0xf
	v_max_f32_dpp v12, v12, v12 quad_perm:[2,3,0,1] row_mask:0xf bank_mask:0xf
	v_max_f32_dpp v9, v9, v9 row_half_mirror row_mask:0xf bank_mask:0xf
	v_max_f32_dpp v10, v10, v10 row_half_mirror row_mask:0xf bank_mask:0xf
	v_max_f32_dpp v11, v11, v11 row_half_mirror row_mask:0xf bank_mask:0xf
	v_max_f32_dpp v12, v12, v12 row_half_mirror row_mask:0xf bank_mask:0xf
	s_and_saveexec_b64 s[0:1], vcc
	s_cbranch_execz .LBB4_18
	v_cvt_pk_f16_f32 v10, v9, v10
	v_cvt_pk_f16_f32 v11, v11, v12
	global_store_dwordx2 v[4:5], v[10:11], off offset:1216
.LBB4_18:
	s_or_b64 exec, exec, s[0:1]
	v_add_u32_e32 v0, 0x20000, v214
	ds_read_b64 v[16:17], v0
	s_waitcnt lgkmcnt(0)
	v_cvt_f32_f16_e32 v9, v16
	v_cvt_f32_f16_sdwa v10, v16 dst_sel:DWORD dst_unused:UNUSED_PAD src0_sel:WORD_1
	v_cvt_f32_f16_e32 v11, v17
	v_cvt_f32_f16_sdwa v12, v17 dst_sel:DWORD dst_unused:UNUSED_PAD src0_sel:WORD_1
	global_store_dwordx2 v[2:3], v[16:17], off offset:1248
	v_max_f32_dpp v9, v9, v9 quad_perm:[1,0,3,2] row_mask:0xf bank_mask:0xf
	v_max_f32_dpp v10, v10, v10 quad_perm:[1,0,3,2] row_mask:0xf bank_mask:0xf
	v_max_f32_dpp v11, v11, v11 quad_perm:[1,0,3,2] row_mask:0xf bank_mask:0xf
	v_max_f32_dpp v12, v12, v12 quad_perm:[1,0,3,2] row_mask:0xf bank_mask:0xf
	v_max_f32_dpp v9, v9, v9 quad_perm:[2,3,0,1] row_mask:0xf bank_mask:0xf
	v_max_f32_dpp v10, v10, v10 quad_perm:[2,3,0,1] row_mask:0xf bank_mask:0xf
	v_max_f32_dpp v11, v11, v11 quad_perm:[2,3,0,1] row_mask:0xf bank_mask:0xf
	v_max_f32_dpp v12, v12, v12 quad_perm:[2,3,0,1] row_mask:0xf bank_mask:0xf
	v_max_f32_dpp v9, v9, v9 row_half_mirror row_mask:0xf bank_mask:0xf
	v_max_f32_dpp v10, v10, v10 row_half_mirror row_mask:0xf bank_mask:0xf
	v_max_f32_dpp v11, v11, v11 row_half_mirror row_mask:0xf bank_mask:0xf
	v_max_f32_dpp v12, v12, v12 row_half_mirror row_mask:0xf bank_mask:0xf
	s_and_saveexec_b64 s[0:1], vcc
	s_cbranch_execz .LBB4_20
	v_cvt_pk_f16_f32 v10, v9, v10
	v_cvt_pk_f16_f32 v11, v11, v12
	global_store_dwordx2 v[4:5], v[10:11], off offset:1248

.LBB8_22:
.LBB8_25:
	s_ashr_i32 s4, s16, 31
	s_lshr_b32 s4, s4, 24
	s_add_i32 s4, s16, s4
	s_ashr_i32 s33, s4, 8
	s_ashr_i32 s4, s17, 31
	s_lshr_b32 s4, s4, 24
	s_add_i32 s4, s17, s4
	s_ashr_i32 s6, s4, 8
	s_mul_i32 s22, s6, s33
	s_cmp_ge_i32 s2, s22
	v_readfirstlane_b32 s36, v0
	s_cbranch_scc1 .LBB8_50
	s_ashr_i32 s23, s22, 31
	s_lshr_b32 s4, s23, 29
	s_add_i32 s4, s22, s4
	s_ashr_i32 s37, s4, 3
	s_and_b32 s4, s4, -8
	s_ashr_i32 s39, s2, 31
	s_load_dwordx2 s[12:13], s[0:1], 0x28
	s_sub_i32 s38, s22, s4
	s_lshr_b32 s4, s39, 29
	s_add_i32 s15, s2, s4
	s_and_b32 s4, s15, -8
	s_sub_i32 s14, s2, s4
	s_add_i32 s40, s37, 1
	s_cmp_ge_i32 s14, s38
	s_mul_i32 s41, s40, s38
	s_cbranch_scc0 .LBB8_28
	s_sub_i32 s4, s14, s38
	s_mul_i32 s4, s4, s37
	s_add_i32 s7, s4, s41
	s_ashr_i32 s4, s15, 3
	s_cbranch_execz .LBB8_29
	s_branch .LBB8_30

.LBB8_30:
	v_lshlrev_b32_e32 v2, 10, v178
	s_movk_i32 s5, 0x1c00
	v_and_b32_e32 v0, 8, v178
	v_and_or_b32 v2, v2, s5, v177
	s_movk_i32 s5, 0x70
	s_lshl_b32 s42, s6, 3
	v_and_or_b32 v3, v181, 48, v0
	v_and_or_b32 v0, v179, s5, v0
	s_abs_i32 s43, s42
	v_lshl_or_b32 v170, v0, 7, v176
	v_cvt_f32_u32_e32 v0, s43
	s_add_i32 s4, s7, s4
	s_sub_i32 s7, 0, s43
	s_bfe_i32 s45, s6, 0x1001c
	v_rcp_iflag_f32_e32 v0, v0
	s_abs_i32 s6, s4
	s_lshr_b32 s26, s36, 6
	s_ashr_i32 s19, s18, 31
	v_mul_f32_e32 v0, 0x4f7ffffe, v0
	v_cvt_u32_f32_e32 v0, v0
	s_ashr_i32 s5, s4, 31
	s_lshr_b32 s27, s36, 8
	s_lshl_b64 s[14:15], s[18:19], 8
	v_readfirstlane_b32 s46, v0
	s_mul_i32 s7, s7, s46
	s_mul_hi_u32 s7, s46, s7
	s_add_i32 s46, s46, s7
	s_mul_hi_u32 s7, s6, s46
	s_mul_i32 s20, s7, s43
	s_sub_i32 s6, s6, s20
	s_lshl_b64 s[16:17], s[18:19], 9
	s_lshl_b32 s44, s26, 10
	s_xor_b32 s5, s5, s45
	s_add_i32 s20, s7, 1
	s_sub_i32 s21, s6, s43
	s_cmp_ge_u32 s6, s43
	s_cselect_b32 s7, s20, s7
	s_cselect_b32 s6, s21, s6
	s_add_i32 s20, s7, 1
	s_cmp_ge_u32 s6, s43
	s_cselect_b32 s6, s20, s7
	s_xor_b32 s6, s6, s5
	s_sub_i32 s5, s6, s5
	s_lshl_b32 s6, s5, 3
	s_sub_i32 s7, s33, s6
	s_min_i32 s7, s7, 8
	s_abs_i32 s20, s7
	v_cvt_f32_u32_e32 v0, s20
	s_sub_i32 s24, 0, s20
	s_mul_i32 s5, s5, s42
	s_movk_i32 s21, 0x2000
	v_rcp_iflag_f32_e32 v0, v0
	s_sub_i32 s4, s4, s5
	v_lshlrev_b32_e32 v169, 1, v2
	v_and_or_b32 v2, v175, s21, v2
	v_mul_f32_e32 v0, 0x4f7ffffe, v0
	v_cvt_u32_f32_e32 v0, v0
	s_abs_i32 s21, s4
	s_xor_b32 s5, s4, s7
	s_ashr_i32 s5, s5, 31
	v_readfirstlane_b32 s25, v0
	s_mul_i32 s24, s24, s25
	s_mul_hi_u32 s24, s25, s24
	s_add_i32 s25, s25, s24
	s_mul_hi_u32 s24, s21, s25
	s_mul_i32 s25, s24, s20
	s_sub_i32 s21, s21, s25
	s_add_i32 s25, s24, 1
	s_sub_i32 s28, s21, s20
	s_cmp_ge_u32 s21, s20
	s_cselect_b32 s24, s25, s24
	s_cselect_b32 s21, s28, s21
	s_add_i32 s25, s24, 1
	s_cmp_ge_u32 s21, s20
	s_cselect_b32 s20, s25, s24
	s_xor_b32 s20, s20, s5
	s_sub_i32 s58, s20, s5
	s_mul_i32 s5, s58, s7
	s_sub_i32 s4, s4, s5
	s_add_i32 s57, s4, s6
	s_ashr_i32 s4, s58, 31
	s_mul_i32 s4, s16, s4
	s_mul_hi_u32 s5, s16, s58
	s_add_i32 s6, s5, s4
	s_lshr_b64 s[4:5], s[18:19], 23
	s_mul_i32 s4, s4, s58
	s_add_i32 s6, s6, s4
	s_mul_i32 s4, s16, s58
	s_waitcnt lgkmcnt(0)
	s_add_u32 s24, s12, s4
	s_addc_u32 s25, s13, s6
	s_lshl_b32 s4, s57, 14
	s_ashr_i32 s5, s4, 31
	s_lshl_b64 s[4:5], s[4:5], 1
	s_add_u32 s4, s8, s4
	s_addc_u32 s5, s9, s5
	s_lshl_b32 s6, s57, 15
	v_mul_lo_u32 v4, s18, v182
	v_lshl_or_b32 v168, v3, 7, v176
	v_mul_lo_u32 v3, s18, v180
	s_ashr_i32 s7, s6, 31
	v_add_lshl_u32 v160, v4, v177, 1
	v_add_lshl_u32 v162, v3, v177, 1
	v_lshlrev_b32_e32 v171, 1, v2
	s_lshl_b64 s[6:7], s[6:7], 1
	s_nop 4
	global_load_dwordx4 v[2:5], v168, s[4:5]
	s_add_u32 s6, s10, s6
	global_load_dwordx4 v[6:9], v170, s[4:5]
	s_addc_u32 s7, s11, s7
	global_load_dwordx4 v[10:13], v169, s[6:7]
	s_add_i32 s34, s44, 0
	global_load_dwordx4 v[14:17], v171, s[6:7]
	s_cmp_eq_u32 s83, 0
	s_cbranch_scc1 .Lgt_nobar
	s_waitcnt vmcnt(4)
	s_cmpk_gt_u32 s36, 0xff
	s_cbranch_scc1 .Lgt_b1
	s_barrier

.Lgt_nobar:
	s_add_i32 m0, s34, 0x10000
	v_add_u32_e32 v175, 0, v1
	global_load_lds_dwordx4 v160, s[24:25]
	s_add_i32 m0, s34, 0x12000
	s_add_u32 s20, s4, 0x4000
	global_load_lds_dwordx4 v162, s[24:25]
	v_mov_b32_e32 v24, 0
	v_mov_b32_e32 v25, 0
	v_mov_b32_e32 v26, 0
	v_mov_b32_e32 v27, 0
	v_mov_b32_e32 v28, 0
	v_mov_b32_e32 v29, 0
	v_mov_b32_e32 v30, 0
	v_mov_b32_e32 v31, 0
	v_mov_b32_e32 v32, 0
	v_mov_b32_e32 v33, 0
	v_mov_b32_e32 v34, 0
	v_mov_b32_e32 v35, 0
	v_mov_b32_e32 v36, 0
	v_mov_b32_e32 v37, 0
	v_mov_b32_e32 v38, 0
	v_mov_b32_e32 v39, 0
	v_mov_b32_e32 v40, 0
	v_mov_b32_e32 v41, 0
	v_mov_b32_e32 v42, 0
	v_mov_b32_e32 v43, 0
	v_mov_b32_e32 v44, 0
	v_mov_b32_e32 v45, 0
	v_mov_b32_e32 v46, 0
	v_mov_b32_e32 v47, 0
	v_mov_b32_e32 v48, 0
	v_mov_b32_e32 v49, 0
	v_mov_b32_e32 v50, 0
	v_mov_b32_e32 v51, 0
	v_mov_b32_e32 v52, 0
	v_mov_b32_e32 v53, 0
	v_mov_b32_e32 v54, 0
	v_mov_b32_e32 v55, 0
	v_mov_b32_e32 v56, 0
	v_mov_b32_e32 v57, 0
	v_mov_b32_e32 v58, 0
	v_mov_b32_e32 v59, 0
	v_mov_b32_e32 v60, 0
	v_mov_b32_e32 v61, 0
	v_mov_b32_e32 v62, 0
	v_mov_b32_e32 v63, 0
	v_mov_b32_e32 v64, 0
	v_mov_b32_e32 v65, 0
	v_mov_b32_e32 v66, 0
	v_mov_b32_e32 v67, 0
	v_mov_b32_e32 v68, 0
	v_mov_b32_e32 v69, 0
	v_mov_b32_e32 v70, 0
	v_mov_b32_e32 v71, 0
	v_mov_b32_e32 v72, 0
	v_mov_b32_e32 v73, 0
	v_mov_b32_e32 v74, 0
	v_mov_b32_e32 v75, 0
	v_mov_b32_e32 v76, 0
	v_mov_b32_e32 v77, 0
	v_mov_b32_e32 v78, 0
	v_mov_b32_e32 v79, 0
	v_mov_b32_e32 v80, 0
	v_mov_b32_e32 v81, 0
	v_mov_b32_e32 v82, 0
	v_mov_b32_e32 v83, 0
	v_mov_b32_e32 v84, 0
	v_mov_b32_e32 v85, 0
	v_mov_b32_e32 v86, 0
	v_mov_b32_e32 v87, 0
	v_mov_b32_e32 v88, 0
	v_mov_b32_e32 v89, 0
	v_mov_b32_e32 v90, 0
	v_mov_b32_e32 v91, 0
	v_mov_b32_e32 v92, 0
	v_mov_b32_e32 v93, 0
	v_mov_b32_e32 v94, 0
	v_mov_b32_e32 v95, 0
	v_mov_b32_e32 v96, 0
	v_mov_b32_e32 v97, 0
	v_mov_b32_e32 v98, 0
	v_mov_b32_e32 v99, 0
	v_mov_b32_e32 v100, 0
	v_mov_b32_e32 v101, 0
	v_mov_b32_e32 v102, 0
	v_mov_b32_e32 v103, 0
	v_mov_b32_e32 v104, 0
	v_mov_b32_e32 v105, 0
	v_mov_b32_e32 v106, 0
	v_mov_b32_e32 v107, 0
	v_mov_b32_e32 v108, 0
	v_mov_b32_e32 v109, 0
	v_mov_b32_e32 v110, 0
	v_mov_b32_e32 v111, 0
	v_mov_b32_e32 v112, 0
	v_mov_b32_e32 v113, 0
	v_mov_b32_e32 v114, 0
	v_mov_b32_e32 v115, 0
	v_mov_b32_e32 v116, 0
	v_mov_b32_e32 v117, 0
	v_mov_b32_e32 v118, 0
	v_mov_b32_e32 v119, 0
	v_mov_b32_e32 v120, 0
	v_mov_b32_e32 v121, 0
	v_mov_b32_e32 v122, 0
	v_mov_b32_e32 v123, 0
	v_mov_b32_e32 v124, 0
	v_mov_b32_e32 v125, 0
	v_mov_b32_e32 v126, 0
	v_mov_b32_e32 v127, 0
	v_mov_b32_e32 v128, 0
	v_mov_b32_e32 v129, 0
	v_mov_b32_e32 v130, 0
	v_mov_b32_e32 v131, 0
	v_mov_b32_e32 v132, 0
	v_mov_b32_e32 v133, 0
	v_mov_b32_e32 v134, 0
	v_mov_b32_e32 v135, 0
	v_mov_b32_e32 v136, 0
	v_mov_b32_e32 v137, 0
	v_mov_b32_e32 v138, 0
	v_mov_b32_e32 v139, 0
	v_mov_b32_e32 v140, 0
	v_mov_b32_e32 v141, 0
	v_mov_b32_e32 v142, 0
	v_mov_b32_e32 v143, 0
	s_waitcnt vmcnt(2)
	s_addc_u32 s21, s5, 0
	v_pk_add_f16 v0, v2, v10
	v_pk_add_f16 v2, v3, v11
	v_pk_add_f16 v3, v4, v12
	v_pk_add_f16 v4, v5, v13
	s_add_u32 s28, s6, 0x8000
	v_pk_max_f16 v5, v4, 0
	v_pk_max_f16 v4, v3, 0
	v_pk_max_f16 v3, v2, 0
	v_pk_max_f16 v2, v0, 0
	v_pk_add_f16 v0, v6, v14
	v_pk_add_f16 v6, v7, v15
	v_pk_add_f16 v7, v8, v16
	v_pk_add_f16 v8, v9, v17
	s_addc_u32 s29, s7, 0
	v_pk_max_f16 v9, v8, 0
	v_pk_max_f16 v8, v7, 0
	v_pk_max_f16 v7, v6, 0
	v_pk_max_f16 v6, v0, 0
	ds_write_b128 v175, v[2:5]
	ds_write_b128 v175, v[6:9] offset:8192
	s_nop 4
	global_load_dwordx4 v[0:3], v168, s[20:21]
	global_load_dwordx4 v[4:7], v170, s[20:21]
	global_load_dwordx4 v[8:11], v169, s[28:29]
	s_add_u32 s20, s24, s14
	global_load_dwordx4 v[12:15], v171, s[28:29]
	s_addc_u32 s21, s25, s15
	s_add_i32 m0, s34, 0x14000
	v_mov_b32_e32 v161, 0
	global_load_lds_dwordx4 v160, s[20:21]
	s_add_i32 m0, s34, 0x16000
	s_add_u32 s28, s4, 0x80
	global_load_lds_dwordx4 v162, s[20:21]
	s_waitcnt vmcnt(2)
	s_addc_u32 s29, s5, 0
	v_pk_add_f16 v0, v0, v8
	v_pk_add_f16 v1, v1, v9
	v_pk_add_f16 v2, v2, v10
	v_pk_add_f16 v3, v3, v11
	v_pk_max_f16 v2, v2, 0
	v_pk_max_f16 v3, v3, 0
	v_pk_max_f16 v1, v1, 0
	v_pk_max_f16 v0, v0, 0
	v_pk_add_f16 v4, v4, v12
	v_pk_add_f16 v5, v5, v13
	v_pk_add_f16 v6, v6, v14
	v_pk_add_f16 v7, v7, v15
	v_pk_max_f16 v6, v6, 0
	v_pk_max_f16 v7, v7, 0
	v_pk_max_f16 v5, v5, 0
	v_pk_max_f16 v4, v4, 0
	ds_write_b128 v175, v[0:3] offset:16384
	ds_write_b128 v175, v[4:7] offset:24576
	s_nop 4
	global_load_dwordx4 v[0:3], v168, s[28:29]
	v_mov_b32_e32 v163, v161
	s_add_u32 s30, s6, 0x80
	global_load_dwordx4 v[4:7], v170, s[28:29]
	v_lshl_add_u64 v[18:19], s[24:25], 0, v[160:161]
	v_lshl_add_u64 v[16:17], s[20:21], 0, v[160:161]
	v_lshl_add_u64 v[22:23], s[20:21], 0, v[162:163]
	s_mov_b64 s[20:21], 0x80
	s_addc_u32 s31, s7, 0
	global_load_dwordx4 v[8:11], v169, s[30:31]
	v_lshl_add_u64 v[20:21], s[24:25], 0, v[162:163]
	global_load_dwordx4 v[12:15], v171, s[30:31]
	s_add_i32 m0, s34, 0x18000
	v_lshl_add_u64 v[18:19], v[18:19], 0, s[20:21]
	global_load_lds_dwordx4 v[18:19], off
	v_lshl_add_u64 v[18:19], v[20:21], 0, s[20:21]
	s_add_i32 m0, s34, 0x1a000
	s_add_u32 s4, s4, 0x4080
	global_load_lds_dwordx4 v[18:19], off
	s_waitcnt vmcnt(2)
	s_addc_u32 s5, s5, 0
	v_pk_add_f16 v0, v0, v8
	v_pk_add_f16 v1, v1, v9
	v_pk_add_f16 v2, v2, v10
	v_pk_add_f16 v3, v3, v11
	v_pk_max_f16 v2, v2, 0
	v_pk_max_f16 v3, v3, 0
	v_pk_max_f16 v1, v1, 0
	v_pk_max_f16 v0, v0, 0
	v_pk_add_f16 v4, v4, v12
	v_pk_add_f16 v5, v5, v13
	v_pk_add_f16 v6, v6, v14
	v_pk_add_f16 v7, v7, v15
	v_pk_max_f16 v6, v6, 0
	v_pk_max_f16 v7, v7, 0
	v_pk_max_f16 v5, v5, 0
	v_pk_max_f16 v4, v4, 0
	ds_write_b128 v175, v[0:3] offset:32768
	ds_write_b128 v175, v[4:7] offset:40960
	s_nop 4
	global_load_dwordx4 v[8:11], v168, s[4:5]
	s_add_u32 s6, s6, 0x8080
	global_load_dwordx4 v[0:3], v170, s[4:5]
	s_addc_u32 s7, s7, 0
	global_load_dwordx4 v[12:15], v169, s[6:7]
	global_load_dwordx4 v[4:7], v171, s[6:7]
	s_add_i32 m0, s34, 0x1c000
	v_lshl_add_u64 v[16:17], v[16:17], 0, s[20:21]
	global_load_lds_dwordx4 v[16:17], off
	v_lshl_add_u64 v[16:17], v[22:23], 0, s[20:21]
	s_add_i32 m0, s34, 0x1e000
	s_cmp_lg_u32 s27, 1
	global_load_lds_dwordx4 v[16:17], off
	s_load_dwordx4 s[4:7], s[0:1], 0x68
	s_load_dword s47, s[0:1], 0x78
	s_mov_b32 s48, 0
	s_cbranch_scc1 .LBB8_32
	s_barrier
